# adds P4: all four heads component loads issued together per row, subln_g once per row
# speedup vs baseline: 1.0036x; 1.0036x over previous
; __device__ __forceinline__ unsigned pk2(float lo, float hi) { return f2bf(lo) | (f2bf(hi) << 16); }
; __device__ __forceinline__ void p4_finalize(Frame& F, const Args& A) {
;     ...
;         { const int h = F.lane >> 3; const float l0 = LS[((size_t)0 * T + m) * 8 + h], l1 = LS[((size_t)1 * T + m) * 8 + h], l2 = LS[((size_t)2 * T + m) * 8 + h];
;           const float mx = fmaxf(l0, fmaxf(l1, l2)); float w0 = __expf(l0 - mx), w1 = __expf(l1 - mx), w2 = __expf(l2 - mx); const float inv = 1.0f / (w0 + w1 + w2); w0 *= inv; w1 *= inv; w2 *= inv;
;           const size_t o = (size_t)m * 1024 + 16 * F.lane; unsigned pk[8];
; #pragma unroll
;           for (int q = 0; q < 2; ++q) { const v4u a0 = *(const v4u*)(OA + o + 8 * q), a1 = *(const v4u*)(OA + (size_t)T * 1024 + o + 8 * q), a2 = *(const v4u*)(OA + (size_t)2 * T * 1024 + o + 8 * q);
; #pragma unroll
;               for (int e = 0; e < 4; ++e) { const float ylo = w0 * __uint_as_float(a0[e] << 16) + w1 * __uint_as_float(a1[e] << 16) + w2 * __uint_as_float(a2[e] << 16);
;                   const float yhi = w0 * __uint_as_float(a0[e] & 0xffff0000u) + w1 * __uint_as_float(a1[e] & 0xffff0000u) + w2 * __uint_as_float(a2[e] & 0xffff0000u); pk[4 * q + e] = pk2(ylo, yhi); } }
.LBB0_661:
	v_lshl_add_u64 v[22:23], s[30:31], 0, v[14:15]
	v_add_co_u32_e64 v48, s[4:5], s0, v22
	v_lshl_add_u64 v[26:27], s[30:31], 0, v[10:11]
	s_nop 0
	v_addc_co_u32_e64 v49, s[4:5], 0, v23, s[4:5]
	v_add_co_u32_e64 v42, s[4:5], s1, v22
	v_lshl_add_u64 v[28:29], s[30:31], 0, v[18:19]
	s_nop 0
	v_addc_co_u32_e64 v43, s[4:5], 0, v23, s[4:5]
	v_add_co_u32_e64 v52, s[4:5], s2, v22
	v_add_co_u32_e32 v60, vcc, 0x1a000000, v28
	s_nop 0
	v_addc_co_u32_e64 v53, s[4:5], 0, v23, s[4:5]
	v_add_co_u32_e64 v24, s[4:5], s9, v26
	v_addc_co_u32_e32 v61, vcc, 0, v29, vcc
	s_nop 0
	v_addc_co_u32_e64 v25, s[4:5], 0, v27, s[4:5]
	v_add_co_u32_e64 v26, s[4:5], s10, v26
	v_lshl_add_u64 v[40:41], s[30:31], 0, v[12:13]
	s_nop 0
	v_addc_co_u32_e64 v27, s[4:5], 0, v27, s[4:5]
	v_add_co_u32_e32 v64, vcc, 0x1a040000, v28
	v_lshl_add_u64 v[62:63], v[22:23], 0, s[38:39]
	v_lshl_add_u64 v[44:45], v[22:23], 0, s[40:41]
	v_lshl_add_u64 v[56:57], v[22:23], 0, s[42:43]
	v_add_co_u32_e64 v22, s[4:5], s15, v40
	v_addc_co_u32_e32 v65, vcc, 0, v29, vcc
	s_nop 0
	v_addc_co_u32_e64 v23, s[4:5], 0, v41, s[4:5]
	global_load_dwordx4 v[40:43], v[42:43], off
	s_nop 0
	global_load_dwordx4 v[44:47], v[44:45], off offset:16
	s_nop 0
	global_load_dwordx4 v[48:51], v[48:49], off
	s_nop 0
	global_load_dwordx4 v[52:55], v[52:53], off
	s_nop 0
	global_load_dwordx4 v[56:59], v[56:57], off offset:16
	s_nop 0
	global_load_dword v75, v[60:61], off
	v_add_co_u32_e32 v28, vcc, 0x1a080000, v28
	v_mov_b32_e32 v2, 0
	s_nop 0
	v_addc_co_u32_e32 v29, vcc, 0, v29, vcc
	global_load_dword v76, v[64:65], off
	global_load_dword v77, v[28:29], off
	s_nop 0
	global_load_dwordx4 v[60:63], v[62:63], off offset:16
	v_mov_b32_e32 v3, 0
	v_mov_b32_e32 v4, 0
	v_mov_b32_e32 v5, 0
	v_lshl_add_u64 v[30:31], s[30:31], 0, v[16:17]
	v_mov_b32_e32 v74, 0
	s_add_i32 s8, s8, s14
	v_lshl_add_u64 v[10:11], v[10:11], 0, s[18:19]
	v_lshl_add_u64 v[12:13], v[12:13], 0, s[22:23]
	v_lshl_add_u64 v[14:15], v[14:15], 0, s[18:19]
	v_lshl_add_u64 v[16:17], v[16:17], 0, s[22:23]
	v_lshl_add_u64 v[18:19], v[18:19], 0, s[36:37]
	s_cmpk_lt_i32 s8, 0x2000
	s_waitcnt vmcnt(8)
	v_lshlrev_b32_e32 v78, 16, v40
	v_and_b32_e32 v79, 0xffff0000, v40
	v_lshlrev_b32_e32 v80, 16, v41
	v_and_b32_e32 v81, 0xffff0000, v41
	v_lshlrev_b32_e32 v82, 16, v42
	v_and_b32_e32 v83, 0xffff0000, v42
	v_lshlrev_b32_e32 v84, 16, v43
	v_and_b32_e32 v85, 0xffff0000, v43
	s_waitcnt vmcnt(7)
	v_lshlrev_b32_e32 v86, 16, v44
	s_waitcnt vmcnt(1)
	v_max3_f32 v94, v75, v76, v77
	v_and_b32_e32 v87, 0xffff0000, v44
	v_lshlrev_b32_e32 v88, 16, v45
	v_and_b32_e32 v89, 0xffff0000, v45
	v_lshlrev_b32_e32 v90, 16, v46
	v_and_b32_e32 v91, 0xffff0000, v46
	v_lshlrev_b32_e32 v92, 16, v47
	v_lshlrev_b32_e32 v29, 16, v48
	v_lshlrev_b32_e32 v28, 16, v52
	v_and_b32_e32 v41, 0xffff0000, v48
	v_and_b32_e32 v40, 0xffff0000, v52
	v_lshlrev_b32_e32 v43, 16, v49
	v_lshlrev_b32_e32 v42, 16, v53
	v_and_b32_e32 v45, 0xffff0000, v49
	v_and_b32_e32 v44, 0xffff0000, v53
	v_lshlrev_b32_e32 v49, 16, v50
	v_lshlrev_b32_e32 v48, 16, v54
	v_and_b32_e32 v53, 0xffff0000, v50
	v_and_b32_e32 v52, 0xffff0000, v54
	v_lshlrev_b32_e32 v64, 16, v55
	v_and_b32_e32 v50, 0xffff0000, v55
	v_lshlrev_b32_e32 v46, 16, v56
	v_and_b32_e32 v54, 0xffff0000, v56
	v_lshlrev_b32_e32 v56, 16, v57
	v_and_b32_e32 v66, 0xffff0000, v57
	v_and_b32_e32 v93, 0xffff0000, v47
	s_waitcnt vmcnt(0)
	v_lshlrev_b32_e32 v47, 16, v60
	v_and_b32_e32 v55, 0xffff0000, v60
	v_lshlrev_b32_e32 v57, 16, v61
	v_and_b32_e32 v67, 0xffff0000, v61
	v_sub_f32_e32 v60, v75, v94
	v_sub_f32_e32 v61, v76, v94
	v_lshlrev_b32_e32 v70, 16, v59
	v_and_b32_e32 v72, 0xffff0000, v59
	v_lshlrev_b32_e32 v69, 16, v62
	v_and_b32_e32 v59, 0xffff0000, v62
	v_lshlrev_b32_e32 v71, 16, v63
	v_and_b32_e32 v73, 0xffff0000, v63
	v_sub_f32_e32 v62, v77, v94
	v_mul_f32_e32 v60, 0x3fb8aa3b, v60
	v_mul_f32_e32 v63, 0x3fb8aa3b, v61
	v_mul_f32_e32 v62, 0x3fb8aa3b, v62
	v_exp_f32_e32 v61, v60
	v_exp_f32_e32 v63, v63
	v_exp_f32_e32 v60, v62
	v_lshlrev_b32_e32 v65, 16, v51
	v_and_b32_e32 v51, 0xffff0000, v51
	v_add_f32_e32 v62, v61, v63
	v_add_f32_e32 v62, v60, v62
	v_div_scale_f32 v75, s[4:5], v62, v62, 1.0
	v_rcp_f32_e32 v77, v75
	v_div_scale_f32 v76, vcc, 1.0, v62, 1.0
	v_lshlrev_b32_e32 v68, 16, v58
	v_fma_f32 v94, -v75, v77, 1.0
	v_fmac_f32_e32 v77, v94, v77
	v_mul_f32_e32 v94, v76, v77
	v_fma_f32 v95, -v75, v94, v76
	v_fmac_f32_e32 v94, v95, v77
	v_fma_f32 v75, -v75, v94, v76
	v_div_fmas_f32 v75, v75, v77, v94
	v_div_fixup_f32 v62, v75, v62, 1.0
	v_and_b32_e32 v58, 0xffff0000, v58
	v_pk_mul_f32 v[60:61], v[60:61], v[62:63] op_sel_hi:[1,0]
	v_mul_f32_e32 v75, v63, v62
	v_pk_mul_f32 v[28:29], v[60:61], v[28:29]
	v_pk_mul_f32 v[40:41], v[60:61], v[40:41]
	v_pk_mul_f32 v[42:43], v[60:61], v[42:43]
	v_pk_mul_f32 v[44:45], v[60:61], v[44:45]
	v_pk_mul_f32 v[48:49], v[60:61], v[48:49]
	v_pk_mul_f32 v[52:53], v[60:61], v[52:53]
	v_pk_mul_f32 v[62:63], v[60:61], v[64:65]
	v_pk_mul_f32 v[50:51], v[60:61], v[50:51]
	v_pk_mul_f32 v[46:47], v[60:61], v[46:47]
	v_pk_mul_f32 v[54:55], v[60:61], v[54:55]
	v_pk_mul_f32 v[64:65], v[60:61], v[66:67]
	v_pk_mul_f32 v[66:67], v[60:61], v[68:69]
	v_pk_mul_f32 v[58:59], v[60:61], v[58:59]
	v_fma_f32 v29, v75, v78, v29
	v_fma_f32 v41, v75, v79, v41
	v_fma_f32 v43, v75, v80, v43
	v_fma_f32 v45, v75, v81, v45
	v_fma_f32 v49, v75, v82, v49
	v_fma_f32 v53, v75, v83, v53
	v_fma_f32 v51, v75, v85, v51
	v_fma_f32 v47, v75, v86, v47
	v_fma_f32 v55, v75, v87, v55
	v_fma_f32 v67, v75, v90, v67
	v_fma_f32 v59, v75, v91, v59
	v_fma_f32 v63, v75, v84, v63
	v_add_f32_e32 v28, v28, v29
	v_add_f32_e32 v29, v40, v41
	v_add_f32_e32 v40, v42, v43
	v_add_f32_e32 v41, v44, v45
; __device__ __forceinline__ void p4_finalize(Frame& F, const Args& A) {
;     ...
;               for (int e = 0; e < 4; ++e) { const float ylo = w0 * __uint_as_float(a0[e] << 16) + w1 * __uint_as_float(a1[e] << 16) + w2 * __uint_as_float(a2[e] << 16);
;                   const float yhi = w0 * __uint_as_float(a0[e] & 0xffff0000u) + w1 * __uint_as_float(a1[e] & 0xffff0000u) + w2 * __uint_as_float(a2[e] & 0xffff0000u); pk[4 * q + e] = pk2(ylo, yhi); } }
;           if constexpr (P5_F8) { v4u w8;
; #pragma unroll
;               for (int e = 0; e < 4; ++e) { const unsigned p0 = pk[2 * e], p1 = pk[2 * e + 1];
;                   int w = __builtin_amdgcn_cvt_pk_fp8_f32(__uint_as_float(p0 << 16) * 16.f, __uint_as_float(p0 & 0xffff0000u) * 16.f, 0, false);
;                   w = __builtin_amdgcn_cvt_pk_fp8_f32(__uint_as_float(p1 << 16) * 16.f, __uint_as_float(p1 & 0xffff0000u) * 16.f, w, true); w8[e] = (unsigned)w; }
;               *(v4u*)(WSP(unsigned char, WS_YA) + o) = w8; }
;           else { bf16* ya = WSP(bf16, WS_YA) + o; *(v4u*)ya = (v4u){pk[0], pk[1], pk[2], pk[3]}; *(v4u*)(ya + 8) = (v4u){pk[4], pk[5], pk[6], pk[7]}; } }
; #pragma unroll
;         for (int h = 0; h < 4; ++h) { const size_t o = (size_t)m * 1024 + h * 256 + 4 * F.lane;
;             const v2u b0 = *(const v2u*)(OB + o), b1 = *(const v2u*)(OB + (size_t)T * 1024 + o);
;             const f32x4 v = (f32x4){__uint_as_float(b0.x << 16), __uint_as_float(b0.x & 0xffff0000u), __uint_as_float(b0.y << 16), __uint_as_float(b0.y & 0xffff0000u)}
;                           - (f32x4){__uint_as_float(b1.x << 16), __uint_as_float(b1.x & 0xffff0000u), __uint_as_float(b1.y << 16), __uint_as_float(b1.y & 0xffff0000u)} * lam;
;             const float ss = wave_sum((v.x * v.x + v.y * v.y) + (v.z * v.z + v.w * v.w)); const float rstd = 1.0f / sqrtf(ss * (1.0f / 256.0f) + EPS);
;             const f32x4 g = *(const f32x4*)(A.in[I_SUBG] + 4 * F.lane); const f32x4 y = v * rstd * g * (1.0f - LAMBDA_INIT);
;             if constexpr (P5_F8) { int w = __builtin_amdgcn_cvt_pk_fp8_f32(y.x * 16.f, y.y * 16.f, 0, false); w = __builtin_amdgcn_cvt_pk_fp8_f32(y.z * 16.f, y.w * 16.f, w, true); *(int*)(WSP(unsigned char, WS_YB) + o) = w; }
;             else { v2u w; w.x = pk2(y.x, y.y); w.y = pk2(y.z, y.w); *(v2u*)(WSP(bf16, WS_YB) + o) = w; } }
	v_add_f32_e32 v42, v48, v49
	v_add_f32_e32 v43, v52, v53
	v_add_f32_e32 v45, v50, v51
	v_add_f32_e32 v46, v46, v47
	v_add_f32_e32 v47, v54, v55
	v_add_f32_e32 v50, v66, v67
	v_add_f32_e32 v51, v58, v59
	v_add_f32_e32 v44, v62, v63
	v_bfe_u32 v54, v28, 16, 1
	v_bfe_u32 v55, v29, 16, 1
	v_bfe_u32 v58, v42, 16, 1
	v_bfe_u32 v59, v43, 16, 1
	v_bfe_u32 v62, v46, 16, 1
	v_bfe_u32 v63, v47, 16, 1
	v_bfe_u32 v66, v50, 16, 1
	v_bfe_u32 v67, v51, 16, 1
	v_pk_mul_f32 v[56:57], v[60:61], v[56:57]
	v_pk_mul_f32 v[68:69], v[60:61], v[70:71]
	v_pk_mul_f32 v[60:61], v[60:61], v[72:73]
	v_add3_u32 v28, v28, v54, s3
	v_add3_u32 v29, v29, v55, s3
	v_add3_u32 v42, v42, v58, s3
	v_add3_u32 v43, v43, v59, s3
	v_add3_u32 v46, v46, v62, s3
	v_add3_u32 v47, v47, v63, s3
	v_add3_u32 v50, v50, v66, s3
	v_add3_u32 v51, v51, v67, s3
	v_fma_f32 v57, v75, v88, v57
	v_fma_f32 v65, v75, v89, v65
	v_fma_f32 v69, v75, v92, v69
	v_fma_f32 v61, v75, v93, v61
	v_and_b32_e32 v29, 0xffff0000, v29
	v_and_b32_e32 v43, 0xffff0000, v43
	v_and_b32_e32 v47, 0xffff0000, v47
	v_and_b32_e32 v51, 0xffff0000, v51
	v_and_b32_e32 v28, 0xffff0000, v28
	v_and_b32_e32 v42, 0xffff0000, v42
	v_and_b32_e32 v46, 0xffff0000, v46
	v_and_b32_e32 v50, 0xffff0000, v50
	v_add_f32_e32 v48, v56, v57
	v_add_f32_e32 v49, v64, v65
	v_add_f32_e32 v52, v68, v69
	v_add_f32_e32 v53, v60, v61
	v_mul_f32_e32 v28, 0x41800000, v28
	v_mul_f32_e32 v29, 0x41800000, v29
	v_mul_f32_e32 v42, 0x41800000, v42
	v_mul_f32_e32 v43, 0x41800000, v43
	v_mul_f32_e32 v46, 0x41800000, v46
	v_mul_f32_e32 v47, 0x41800000, v47
	v_mul_f32_e32 v50, 0x41800000, v50
	v_mul_f32_e32 v51, 0x41800000, v51
	v_bfe_u32 v56, v40, 16, 1
	v_bfe_u32 v57, v41, 16, 1
	v_bfe_u32 v60, v44, 16, 1
	v_bfe_u32 v61, v45, 16, 1
	v_bfe_u32 v64, v48, 16, 1
	v_bfe_u32 v65, v49, 16, 1
	v_bfe_u32 v68, v52, 16, 1
	v_bfe_u32 v69, v53, 16, 1
	v_cvt_pk_fp8_f32 v2, v28, v29
	v_cvt_pk_fp8_f32 v3, v42, v43
	v_cvt_pk_fp8_f32 v4, v46, v47
	v_cvt_pk_fp8_f32 v5, v50, v51
	v_add3_u32 v40, v40, v56, s3
	v_add3_u32 v41, v41, v57, s3
	v_add3_u32 v44, v44, v60, s3
	v_add3_u32 v45, v45, v61, s3
	v_add3_u32 v48, v48, v64, s3
	v_add3_u32 v49, v49, v65, s3
	v_add3_u32 v52, v52, v68, s3
	v_add3_u32 v53, v53, v69, s3
	v_and_b32_e32 v41, 0xffff0000, v41
	v_and_b32_e32 v45, 0xffff0000, v45
	v_and_b32_e32 v49, 0xffff0000, v49
	v_and_b32_e32 v53, 0xffff0000, v53
	v_and_b32_e32 v40, 0xffff0000, v40
	v_and_b32_e32 v44, 0xffff0000, v44
	v_and_b32_e32 v48, 0xffff0000, v48
	v_and_b32_e32 v52, 0xffff0000, v52
	v_mul_f32_e32 v40, 0x41800000, v40
	v_mul_f32_e32 v41, 0x41800000, v41
	v_mul_f32_e32 v44, 0x41800000, v44
	v_mul_f32_e32 v45, 0x41800000, v45
	v_mul_f32_e32 v48, 0x41800000, v48
	v_mul_f32_e32 v49, 0x41800000, v49
	v_mul_f32_e32 v52, 0x41800000, v52
	v_mul_f32_e32 v53, 0x41800000, v53
	v_cvt_pk_fp8_f32 v2, v40, v41 op_sel:[0,0,1]
	v_cvt_pk_fp8_f32 v3, v44, v45 op_sel:[0,0,1]
	v_cvt_pk_fp8_f32 v4, v48, v49 op_sel:[0,0,1]
	v_cvt_pk_fp8_f32 v5, v52, v53 op_sel:[0,0,1]
	v_mov_b32_e32 v46, 0
	global_store_dwordx4 v[30:31], v[2:5], off
	global_load_dwordx4 v[100:103], v[6:7], off
	global_load_dwordx2 v[28:29], v[24:25], off
	s_nop 0
	global_load_dwordx2 v[30:31], v[26:27], off
	global_load_dwordx2 v[104:105], v[24:25], off offset:512
	global_load_dwordx2 v[106:107], v[26:27], off offset:512
	global_load_dwordx2 v[108:109], v[24:25], off offset:1024
	global_load_dwordx2 v[110:111], v[26:27], off offset:1024
	global_load_dwordx2 v[112:113], v[24:25], off offset:1536
	global_load_dwordx2 v[114:115], v[26:27], off offset:1536
	s_waitcnt vmcnt(7)
	v_lshlrev_b32_e32 v40, 16, v28
	v_and_b32_e32 v41, 0xffff0000, v28
	v_lshlrev_b32_e32 v28, 16, v29
	v_and_b32_e32 v29, 0xffff0000, v29
	s_waitcnt vmcnt(6)
	v_lshlrev_b32_e32 v42, 16, v30
	v_and_b32_e32 v43, 0xffff0000, v30
	v_lshlrev_b32_e32 v30, 16, v31
	v_and_b32_e32 v31, 0xffff0000, v31
	v_pk_fma_f32 v[40:41], v[8:9], v[42:43], v[40:41] neg_lo:[1,0,0] neg_hi:[1,0,0]
	v_pk_fma_f32 v[28:29], v[20:21], v[30:31], v[28:29]
	v_pk_mul_f32 v[42:43], v[40:41], v[40:41]
	v_pk_mul_f32 v[30:31], v[28:29], v[28:29]
	s_nop 0
	v_pk_mov_b32 v[44:45], v[42:43], v[30:31] op_sel:[1,0]
	v_mov_b32_e32 v43, v31
	v_pk_add_f32 v[30:31], v[44:45], v[42:43]
	s_nop 0
	v_add_f32_e32 v30, v30, v31
	ds_bpermute_b32 v31, v32, v30
	s_waitcnt lgkmcnt(0)
	v_add_f32_e32 v30, v30, v31
	ds_bpermute_b32 v31, v33, v30
	s_waitcnt lgkmcnt(0)
	v_add_f32_e32 v30, v30, v31
	ds_bpermute_b32 v31, v34, v30
	s_waitcnt lgkmcnt(0)
	v_add_f32_e32 v30, v30, v31
	ds_bpermute_b32 v31, v35, v30
	s_waitcnt lgkmcnt(0)
	v_add_f32_e32 v30, v30, v31
	ds_bpermute_b32 v31, v36, v30
	s_waitcnt lgkmcnt(0)
	v_add_f32_e32 v30, v30, v31
	ds_bpermute_b32 v31, v37, v30
	s_waitcnt lgkmcnt(0)
	v_add_f32_e32 v30, v30, v31
	v_fmamk_f32 v30, v30, 0x3b800000, v38
	v_mul_f32_e32 v31, 0x4f800000, v30
	v_cmp_gt_f32_e32 vcc, s11, v30
	s_nop 1
	v_cndmask_b32_e32 v30, v30, v31, vcc
	v_sqrt_f32_e32 v31, v30
	s_nop 0
	v_add_u32_e32 v42, -1, v31
	v_add_u32_e32 v43, 1, v31
	v_fma_f32 v44, -v42, v31, v30
	v_fma_f32 v45, -v43, v31, v30
	v_cmp_ge_f32_e64 s[4:5], 0, v44
	s_nop 1
	v_cndmask_b32_e64 v31, v31, v42, s[4:5]
	v_cmp_lt_f32_e64 s[4:5], 0, v45
	s_nop 1
	v_cndmask_b32_e64 v31, v31, v43, s[4:5]
	v_mul_f32_e32 v42, 0x37800000, v31
	v_cndmask_b32_e32 v31, v31, v42, vcc
	v_cmp_class_f32_e32 vcc, v30, v39
	s_nop 1
	v_cndmask_b32_e32 v30, v31, v30, vcc
	v_div_scale_f32 v31, s[4:5], v30, v30, 1.0
	v_rcp_f32_e32 v43, v31
	v_div_scale_f32 v42, vcc, 1.0, v30, 1.0
	v_fma_f32 v44, -v31, v43, 1.0
	v_fmac_f32_e32 v43, v44, v43
	v_mul_f32_e32 v44, v42, v43
	v_fma_f32 v45, -v31, v44, v42
	v_fmac_f32_e32 v44, v45, v43
	v_fma_f32 v31, -v31, v44, v42
	v_div_fmas_f32 v31, v31, v43, v44
	v_div_fixup_f32 v30, v31, v30, 1.0
	v_pk_mul_f32 v[28:29], v[28:29], v[30:31] op_sel_hi:[1,0]
	v_pk_mul_f32 v[30:31], v[40:41], v[30:31] op_sel_hi:[1,0]
	v_mov_b64_e32 v[2:3], v[100:101]
	v_mov_b64_e32 v[4:5], v[102:103]
	v_pk_mul_f32 v[4:5], v[4:5], v[28:29]
	v_pk_mul_f32 v[2:3], v[2:3], v[30:31]
	v_pk_mul_f32 v[4:5], v[4:5], s[44:45] op_sel_hi:[1,0]
	v_pk_mul_f32 v[2:3], v[2:3], s[44:45] op_sel_hi:[1,0]
	v_mul_f32_e32 v4, 0x41800000, v4
	v_mul_f32_e32 v2, 0x41800000, v2
	v_mul_f32_e32 v3, 0x41800000, v3
	v_cvt_pk_fp8_f32 v74, v2, v3
	v_mul_f32_e32 v5, 0x41800000, v5
	v_cvt_pk_fp8_f32 v74, v4, v5 op_sel:[0,0,1]
	global_store_dword v[22:23], v74, off
	s_nop 1
	s_waitcnt vmcnt(6)
; __device__ __forceinline__ unsigned pk2(float lo, float hi) { return f2bf(lo) | (f2bf(hi) << 16); }
; __device__ __forceinline__ void p4_finalize(Frame& F, const Args& A) {
;     ...
;         for (int h = 0; h < 4; ++h) { const size_t o = (size_t)m * 1024 + h * 256 + 4 * F.lane;
;             const v2u b0 = *(const v2u*)(OB + o), b1 = *(const v2u*)(OB + (size_t)T * 1024 + o);
;             const f32x4 v = (f32x4){__uint_as_float(b0.x << 16), __uint_as_float(b0.x & 0xffff0000u), __uint_as_float(b0.y << 16), __uint_as_float(b0.y & 0xffff0000u)}
;                           - (f32x4){__uint_as_float(b1.x << 16), __uint_as_float(b1.x & 0xffff0000u), __uint_as_float(b1.y << 16), __uint_as_float(b1.y & 0xffff0000u)} * lam;
;             const float ss = wave_sum((v.x * v.x + v.y * v.y) + (v.z * v.z + v.w * v.w)); const float rstd = 1.0f / sqrtf(ss * (1.0f / 256.0f) + EPS);
;             const f32x4 g = *(const f32x4*)(A.in[I_SUBG] + 4 * F.lane); const f32x4 y = v * rstd * g * (1.0f - LAMBDA_INIT);
;             if constexpr (P5_F8) { int w = __builtin_amdgcn_cvt_pk_fp8_f32(y.x * 16.f, y.y * 16.f, 0, false); w = __builtin_amdgcn_cvt_pk_fp8_f32(y.z * 16.f, y.w * 16.f, w, true); *(int*)(WSP(unsigned char, WS_YB) + o) = w; }
;             else { v2u w; w.x = pk2(y.x, y.y); w.y = pk2(y.z, y.w); *(v2u*)(WSP(bf16, WS_YB) + o) = w; } }
	v_mov_b64_e32 v[28:29], v[104:105]
	v_lshlrev_b32_e32 v40, 16, v28
	v_and_b32_e32 v41, 0xffff0000, v28
	v_lshlrev_b32_e32 v28, 16, v29
	v_and_b32_e32 v29, 0xffff0000, v29
	s_waitcnt vmcnt(5)
	v_mov_b64_e32 v[30:31], v[106:107]
	v_lshlrev_b32_e32 v42, 16, v30
	v_and_b32_e32 v43, 0xffff0000, v30
	v_lshlrev_b32_e32 v30, 16, v31
	v_and_b32_e32 v31, 0xffff0000, v31
	v_pk_fma_f32 v[40:41], v[8:9], v[42:43], v[40:41] neg_lo:[1,0,0] neg_hi:[1,0,0]
	v_pk_fma_f32 v[28:29], v[20:21], v[30:31], v[28:29]
	v_pk_mul_f32 v[42:43], v[40:41], v[40:41]
	v_pk_mul_f32 v[30:31], v[28:29], v[28:29]
	s_nop 0
	v_pk_mov_b32 v[44:45], v[42:43], v[30:31] op_sel:[1,0]
	v_mov_b32_e32 v43, v31
	v_pk_add_f32 v[30:31], v[44:45], v[42:43]
	s_nop 0
	v_add_f32_e32 v30, v30, v31
	ds_bpermute_b32 v31, v32, v30
	s_waitcnt lgkmcnt(0)
	v_add_f32_e32 v30, v30, v31
	ds_bpermute_b32 v31, v33, v30
	s_waitcnt lgkmcnt(0)
	v_add_f32_e32 v30, v30, v31
	ds_bpermute_b32 v31, v34, v30
	s_waitcnt lgkmcnt(0)
	v_add_f32_e32 v30, v30, v31
	ds_bpermute_b32 v31, v35, v30
	s_waitcnt lgkmcnt(0)
	v_add_f32_e32 v30, v30, v31
	ds_bpermute_b32 v31, v36, v30
	s_waitcnt lgkmcnt(0)
	v_add_f32_e32 v30, v30, v31
	ds_bpermute_b32 v31, v37, v30
	s_waitcnt lgkmcnt(0)
	v_add_f32_e32 v30, v30, v31
	v_fmamk_f32 v30, v30, 0x3b800000, v38
	v_mul_f32_e32 v31, 0x4f800000, v30
	v_cmp_gt_f32_e32 vcc, s11, v30
	s_nop 1
	v_cndmask_b32_e32 v30, v30, v31, vcc
	v_sqrt_f32_e32 v31, v30
	s_nop 0
	v_add_u32_e32 v42, -1, v31
	v_add_u32_e32 v43, 1, v31
	v_fma_f32 v44, -v42, v31, v30
	v_fma_f32 v45, -v43, v31, v30
	v_cmp_ge_f32_e64 s[4:5], 0, v44
	s_nop 1
	v_cndmask_b32_e64 v31, v31, v42, s[4:5]
	v_cmp_lt_f32_e64 s[4:5], 0, v45
	s_nop 1
	v_cndmask_b32_e64 v31, v31, v43, s[4:5]
	v_mul_f32_e32 v42, 0x37800000, v31
	v_cndmask_b32_e32 v31, v31, v42, vcc
	v_cmp_class_f32_e32 vcc, v30, v39
	s_nop 1
	v_cndmask_b32_e32 v30, v31, v30, vcc
	v_div_scale_f32 v31, s[4:5], v30, v30, 1.0
	v_rcp_f32_e32 v43, v31
	v_div_scale_f32 v42, vcc, 1.0, v30, 1.0
	v_fma_f32 v44, -v31, v43, 1.0
	v_fmac_f32_e32 v43, v44, v43
	v_mul_f32_e32 v44, v42, v43
	v_fma_f32 v45, -v31, v44, v42
	v_fmac_f32_e32 v44, v45, v43
	v_fma_f32 v31, -v31, v44, v42
	v_div_fmas_f32 v31, v31, v43, v44
	v_div_fixup_f32 v30, v31, v30, 1.0
	v_pk_mul_f32 v[28:29], v[28:29], v[30:31] op_sel_hi:[1,0]
	v_pk_mul_f32 v[30:31], v[40:41], v[30:31] op_sel_hi:[1,0]
	v_mov_b64_e32 v[2:3], v[100:101]
	v_mov_b64_e32 v[4:5], v[102:103]
	v_pk_mul_f32 v[4:5], v[4:5], v[28:29]
	v_pk_mul_f32 v[2:3], v[2:3], v[30:31]
	v_pk_mul_f32 v[4:5], v[4:5], s[44:45] op_sel_hi:[1,0]
	v_pk_mul_f32 v[2:3], v[2:3], s[44:45] op_sel_hi:[1,0]
	v_mul_f32_e32 v4, 0x41800000, v4
	v_mul_f32_e32 v2, 0x41800000, v2
	v_mul_f32_e32 v3, 0x41800000, v3
	v_cvt_pk_fp8_f32 v46, v2, v3
	v_mul_f32_e32 v5, 0x41800000, v5
	v_cvt_pk_fp8_f32 v46, v4, v5 op_sel:[0,0,1]
	global_store_dword v[22:23], v46, off offset:256
	s_nop 1
	v_mov_b32_e32 v46, 0
	s_waitcnt vmcnt(5)
	v_mov_b64_e32 v[28:29], v[108:109]
	v_lshlrev_b32_e32 v40, 16, v28
	v_and_b32_e32 v41, 0xffff0000, v28
	v_lshlrev_b32_e32 v28, 16, v29
	v_and_b32_e32 v29, 0xffff0000, v29
	s_waitcnt vmcnt(4)
	v_mov_b64_e32 v[30:31], v[110:111]
	v_lshlrev_b32_e32 v42, 16, v30
	v_and_b32_e32 v43, 0xffff0000, v30
	v_lshlrev_b32_e32 v30, 16, v31
	v_and_b32_e32 v31, 0xffff0000, v31
	v_pk_fma_f32 v[40:41], v[8:9], v[42:43], v[40:41] neg_lo:[1,0,0] neg_hi:[1,0,0]
	v_pk_fma_f32 v[28:29], v[20:21], v[30:31], v[28:29]
	v_pk_mul_f32 v[42:43], v[40:41], v[40:41]
	v_pk_mul_f32 v[30:31], v[28:29], v[28:29]
	s_nop 0
	v_pk_mov_b32 v[44:45], v[42:43], v[30:31] op_sel:[1,0]
	v_mov_b32_e32 v43, v31
	v_pk_add_f32 v[30:31], v[44:45], v[42:43]
	s_nop 0
	v_add_f32_e32 v30, v30, v31
	ds_bpermute_b32 v31, v32, v30
	s_waitcnt lgkmcnt(0)
	v_add_f32_e32 v30, v30, v31
	ds_bpermute_b32 v31, v33, v30
	s_waitcnt lgkmcnt(0)
	v_add_f32_e32 v30, v30, v31
	ds_bpermute_b32 v31, v34, v30
	s_waitcnt lgkmcnt(0)
	v_add_f32_e32 v30, v30, v31
	ds_bpermute_b32 v31, v35, v30
	s_waitcnt lgkmcnt(0)
	v_add_f32_e32 v30, v30, v31
	ds_bpermute_b32 v31, v36, v30
	s_waitcnt lgkmcnt(0)
	v_add_f32_e32 v30, v30, v31
	ds_bpermute_b32 v31, v37, v30
	s_waitcnt lgkmcnt(0)
; __device__ __forceinline__ unsigned pk2(float lo, float hi) { return f2bf(lo) | (f2bf(hi) << 16); }
; __device__ __forceinline__ void p4_finalize(Frame& F, const Args& A) {
;     ...
;         for (int h = 0; h < 4; ++h) { const size_t o = (size_t)m * 1024 + h * 256 + 4 * F.lane;
;             const v2u b0 = *(const v2u*)(OB + o), b1 = *(const v2u*)(OB + (size_t)T * 1024 + o);
;             const f32x4 v = (f32x4){__uint_as_float(b0.x << 16), __uint_as_float(b0.x & 0xffff0000u), __uint_as_float(b0.y << 16), __uint_as_float(b0.y & 0xffff0000u)}
;                           - (f32x4){__uint_as_float(b1.x << 16), __uint_as_float(b1.x & 0xffff0000u), __uint_as_float(b1.y << 16), __uint_as_float(b1.y & 0xffff0000u)} * lam;
;             const float ss = wave_sum((v.x * v.x + v.y * v.y) + (v.z * v.z + v.w * v.w)); const float rstd = 1.0f / sqrtf(ss * (1.0f / 256.0f) + EPS);
;             const f32x4 g = *(const f32x4*)(A.in[I_SUBG] + 4 * F.lane); const f32x4 y = v * rstd * g * (1.0f - LAMBDA_INIT);
;             if constexpr (P5_F8) { int w = __builtin_amdgcn_cvt_pk_fp8_f32(y.x * 16.f, y.y * 16.f, 0, false); w = __builtin_amdgcn_cvt_pk_fp8_f32(y.z * 16.f, y.w * 16.f, w, true); *(int*)(WSP(unsigned char, WS_YB) + o) = w; }
;             else { v2u w; w.x = pk2(y.x, y.y); w.y = pk2(y.z, y.w); *(v2u*)(WSP(bf16, WS_YB) + o) = w; } }
;     }
	v_add_f32_e32 v30, v30, v31
	v_fmamk_f32 v30, v30, 0x3b800000, v38
	v_mul_f32_e32 v31, 0x4f800000, v30
	v_cmp_gt_f32_e32 vcc, s11, v30
	s_nop 1
	v_cndmask_b32_e32 v30, v30, v31, vcc
	v_sqrt_f32_e32 v31, v30
	s_nop 0
	v_add_u32_e32 v42, -1, v31
	v_add_u32_e32 v43, 1, v31
	v_fma_f32 v44, -v42, v31, v30
	v_fma_f32 v45, -v43, v31, v30
	v_cmp_ge_f32_e64 s[4:5], 0, v44
	s_nop 1
	v_cndmask_b32_e64 v31, v31, v42, s[4:5]
	v_cmp_lt_f32_e64 s[4:5], 0, v45
	s_nop 1
	v_cndmask_b32_e64 v31, v31, v43, s[4:5]
	v_mul_f32_e32 v42, 0x37800000, v31
	v_cndmask_b32_e32 v31, v31, v42, vcc
	v_cmp_class_f32_e32 vcc, v30, v39
	s_nop 1
	v_cndmask_b32_e32 v30, v31, v30, vcc
	v_div_scale_f32 v31, s[4:5], v30, v30, 1.0
	v_rcp_f32_e32 v43, v31
	v_div_scale_f32 v42, vcc, 1.0, v30, 1.0
	v_fma_f32 v44, -v31, v43, 1.0
	v_fmac_f32_e32 v43, v44, v43
	v_mul_f32_e32 v44, v42, v43
	v_fma_f32 v45, -v31, v44, v42
	v_fmac_f32_e32 v44, v45, v43
	v_fma_f32 v31, -v31, v44, v42
	v_div_fmas_f32 v31, v31, v43, v44
	v_div_fixup_f32 v30, v31, v30, 1.0
	v_pk_mul_f32 v[28:29], v[28:29], v[30:31] op_sel_hi:[1,0]
	v_pk_mul_f32 v[30:31], v[40:41], v[30:31] op_sel_hi:[1,0]
	v_mov_b64_e32 v[2:3], v[100:101]
	v_mov_b64_e32 v[4:5], v[102:103]
	v_pk_mul_f32 v[4:5], v[4:5], v[28:29]
	v_pk_mul_f32 v[2:3], v[2:3], v[30:31]
	v_pk_mul_f32 v[4:5], v[4:5], s[44:45] op_sel_hi:[1,0]
	v_pk_mul_f32 v[2:3], v[2:3], s[44:45] op_sel_hi:[1,0]
	v_mul_f32_e32 v4, 0x41800000, v4
	v_mul_f32_e32 v2, 0x41800000, v2
	v_mul_f32_e32 v3, 0x41800000, v3
	v_cvt_pk_fp8_f32 v46, v2, v3
	v_mul_f32_e32 v5, 0x41800000, v5
	v_mov_b32_e32 v42, 0
	v_cvt_pk_fp8_f32 v46, v4, v5 op_sel:[0,0,1]
	global_store_dword v[22:23], v46, off offset:512
	s_nop 1
	s_waitcnt vmcnt(4)
	v_mov_b64_e32 v[24:25], v[112:113]
	v_lshlrev_b32_e32 v28, 16, v24
	v_and_b32_e32 v29, 0xffff0000, v24
	v_lshlrev_b32_e32 v24, 16, v25
	v_and_b32_e32 v25, 0xffff0000, v25
	s_waitcnt vmcnt(3)
	v_mov_b64_e32 v[26:27], v[114:115]
	v_lshlrev_b32_e32 v30, 16, v26
	v_and_b32_e32 v31, 0xffff0000, v26
	v_lshlrev_b32_e32 v26, 16, v27
	v_and_b32_e32 v27, 0xffff0000, v27
	v_pk_fma_f32 v[28:29], v[8:9], v[30:31], v[28:29] neg_lo:[1,0,0] neg_hi:[1,0,0]
	v_pk_fma_f32 v[24:25], v[20:21], v[26:27], v[24:25]
	v_pk_mul_f32 v[30:31], v[28:29], v[28:29]
	v_pk_mul_f32 v[26:27], v[24:25], v[24:25]
	s_nop 0
	v_pk_mov_b32 v[40:41], v[30:31], v[26:27] op_sel:[1,0]
	v_mov_b32_e32 v31, v27
	v_pk_add_f32 v[26:27], v[40:41], v[30:31]
	s_nop 0
	v_add_f32_e32 v26, v26, v27
	ds_bpermute_b32 v27, v32, v26
	s_waitcnt lgkmcnt(0)
	v_add_f32_e32 v26, v26, v27
	ds_bpermute_b32 v27, v33, v26
	s_waitcnt lgkmcnt(0)
	v_add_f32_e32 v26, v26, v27
	ds_bpermute_b32 v27, v34, v26
	s_waitcnt lgkmcnt(0)
	v_add_f32_e32 v26, v26, v27
	ds_bpermute_b32 v27, v35, v26
	s_waitcnt lgkmcnt(0)
	v_add_f32_e32 v26, v26, v27
	ds_bpermute_b32 v27, v36, v26
	s_waitcnt lgkmcnt(0)
	v_add_f32_e32 v26, v26, v27
	ds_bpermute_b32 v27, v37, v26
	s_waitcnt lgkmcnt(0)
	v_add_f32_e32 v26, v26, v27
	v_fmamk_f32 v26, v26, 0x3b800000, v38
	v_mul_f32_e32 v27, 0x4f800000, v26
	v_cmp_gt_f32_e32 vcc, s11, v26
	s_nop 1
	v_cndmask_b32_e32 v26, v26, v27, vcc
	v_sqrt_f32_e32 v27, v26
	s_nop 0
	v_add_u32_e32 v30, -1, v27
	v_add_u32_e32 v31, 1, v27
	v_fma_f32 v40, -v30, v27, v26
	v_fma_f32 v41, -v31, v27, v26
	v_cmp_ge_f32_e64 s[4:5], 0, v40
	s_nop 1
	v_cndmask_b32_e64 v27, v27, v30, s[4:5]
	v_cmp_lt_f32_e64 s[4:5], 0, v41
	s_nop 1
	v_cndmask_b32_e64 v27, v27, v31, s[4:5]
	v_mul_f32_e32 v30, 0x37800000, v27
	v_cndmask_b32_e32 v27, v27, v30, vcc
	v_cmp_class_f32_e32 vcc, v26, v39
	s_nop 1
	v_cndmask_b32_e32 v26, v27, v26, vcc
	v_div_scale_f32 v27, s[4:5], v26, v26, 1.0
	v_rcp_f32_e32 v31, v27
	v_div_scale_f32 v30, vcc, 1.0, v26, 1.0
	v_fma_f32 v40, -v27, v31, 1.0
	v_fmac_f32_e32 v31, v40, v31
	v_mul_f32_e32 v40, v30, v31
	v_fma_f32 v41, -v27, v40, v30
	v_fmac_f32_e32 v40, v41, v31
	v_fma_f32 v27, -v27, v40, v30
	v_div_fmas_f32 v27, v27, v31, v40
	v_div_fixup_f32 v26, v27, v26, 1.0
	v_pk_mul_f32 v[24:25], v[24:25], v[26:27] op_sel_hi:[1,0]
	v_pk_mul_f32 v[26:27], v[28:29], v[26:27] op_sel_hi:[1,0]
	v_mov_b64_e32 v[2:3], v[100:101]
	v_mov_b64_e32 v[4:5], v[102:103]
	v_pk_mul_f32 v[4:5], v[4:5], v[24:25]
	v_pk_mul_f32 v[2:3], v[2:3], v[26:27]
	s_nop 0
	v_pk_mul_f32 v[2:3], v[2:3], s[44:45] op_sel_hi:[1,0]
	s_nop 0
	v_mul_f32_e32 v2, 0x41800000, v2
	v_mul_f32_e32 v3, 0x41800000, v3
	v_cvt_pk_fp8_f32 v42, v2, v3
	v_pk_mul_f32 v[2:3], v[4:5], s[44:45] op_sel_hi:[1,0]
	s_nop 0
	v_mul_f32_e32 v2, 0x41800000, v2
	v_mul_f32_e32 v3, 0x41800000, v3
	v_cvt_pk_fp8_f32 v42, v2, v3 op_sel:[0,0,1]
	global_store_dword v[22:23], v42, off offset:768
	s_cbranch_scc1 .LBB0_661
